# RWKV chain loop and its package loaders rewritten by hand (three packages in flight per loader wave)
# baseline (speedup 1.0000x reference)
; #define LAS __attribute__((address_space(3)))
; DI void rk_pkg_fetch(u32x4_t (&buf)[13], const unsigned char* pkg, int lane) {
; #pragma unroll
;     for (int i = 0; i < 12; ++i) buf[i] = __builtin_nontemporal_load((const u32x4_t*)(pkg + i * 1024 + lane * 16));
;     buf[12] = (lane < 16) ? __builtin_nontemporal_load((const u32x4_t*)(pkg + 12288 + lane * 16)) : (u32x4_t){0u, 0u, 0u, 0u};
; }
; DI void rwkv_r2_unit(const Args& A, LAS unsigned char* lds, int u, int tid, int wave, int lane) {
;     bf16* yb = (bf16*)(A.ws + WS_RKY);
;     const int dir = u / 48, rem = u % 48, b = rem / 6, hh = rem % 6; const int fr = lane & 15, qd = lane >> 4;
;     const unsigned char* pkg0 = A.ws + WS_PKG + ((size_t)((dir * NB + b) * 6 + hh) * 128) * PKG_BYTES;
;     volatile LAS unsigned* ready = (volatile LAS unsigned*)(lds + R2_CTL); volatile LAS unsigned* consumed = ready + 8;
;     __syncthreads();
;     if (tid < 16) ready[tid] = 0u;
;     __syncthreads();
;     if (wave >= 4) {
;         const int j = wave - 4; u32x4_t cur[13], nxt[13];
;         rk_pkg_fetch(cur, pkg0 + (size_t)j * PKG_BYTES, lane);
;         for (int cc = j; cc < 128; cc += 4) {
;             if (cc + 4 < 128) rk_pkg_fetch(nxt, pkg0 + (size_t)(cc + 4) * PKG_BYTES, lane);
;             if (cc >= R2_SLOTS) { const unsigned need = (unsigned)(cc - R2_SLOTS + 1); unsigned spins = 0;
;                 for (;;) { const unsigned c0 = consumed[0], c1 = consumed[1], c2 = consumed[2], c3 = consumed[3];
;                     if (c0 >= need && c1 >= need && c2 >= need && c3 >= need) break; if (++spins > (1u << 22)) break; __builtin_amdgcn_s_sleep(1); } }
;             LAS unsigned char* slot = lds + (cc & (R2_SLOTS - 1)) * PKG_BYTES;
; #pragma unroll
;             for (int i = 0; i < 12; ++i) *(LAS u32x4_t*)(slot + i * 1024 + lane * 16) = cur[i];
;             if (lane < 16) *(LAS u32x4_t*)(slot + 12288 + lane * 16) = cur[12];
;             asm volatile("s_waitcnt lgkmcnt(0)" ::: "memory");
;             if (lane == 0) ready[cc & (R2_SLOTS - 1)] = (unsigned)(cc + 1);
;             asm volatile("" ::: "memory");
; #pragma unroll
;             for (int i = 0; i < 13; ++i) cur[i] = nxt[i];
;         }
.LBB0_681:
	s_and_b64 vcc, exec, s[10:11]
	s_cbranch_vccz .LBB0_642
	s_lshl_b32 s10, s14, 3
	s_add_i32 s10, s10, s31
	s_mul_i32 s10, s10, 6
	s_add_i32 s10, s10, s33
	s_mul_hi_i32 s11, s10, 0x188000
	s_mul_i32 s10, s10, 0x188000
	s_add_u32 s16, s24, s10
	s_addc_u32 s17, s25, s11
	s_mul_i32 s10, s23, 0x3100
	s_add_u32 s10, s16, s10
	s_mul_hi_u32 s11, s23, 0x3100
	s_addc_u32 s11, s17, s11
	v_readlane_b32 s18, v235, 52
	v_cmp_eq_u32_e64 s[72:73], 0, v146
	v_cmp_gt_u32_e64 s[74:75], 16, v146
	s_mov_b64 s[42:43], 0x1000
	s_nop 2
	s_add_i32 s18, s18, -4
	s_waitcnt vmcnt(0)
	s_mul_i32 s40, s18, 0x3100
	s_mul_hi_u32 s41, s18, 0x3100
	s_add_u32 s40, s16, s40
	s_addc_u32 s41, s17, s41
	v_lshl_add_u64 v[224:225], s[40:41], 0, v[148:149]
	global_load_dwordx4 v[6:9], v[224:225], off nt
	global_load_dwordx4 v[10:13], v[224:225], off offset:1024 nt
	global_load_dwordx4 v[14:17], v[224:225], off offset:2048 nt
	global_load_dwordx4 v[18:21], v[224:225], off offset:3072 nt
	v_lshl_add_u64 v[224:225], v[224:225], 0, s[42:43]
	global_load_dwordx4 v[22:25], v[224:225], off nt
	global_load_dwordx4 v[26:29], v[224:225], off offset:1024 nt
	global_load_dwordx4 v[30:33], v[224:225], off offset:2048 nt
	global_load_dwordx4 v[34:37], v[224:225], off offset:3072 nt
	v_lshl_add_u64 v[224:225], v[224:225], 0, s[42:43]
	global_load_dwordx4 v[38:41], v[224:225], off nt
	global_load_dwordx4 v[42:45], v[224:225], off offset:1024 nt
	global_load_dwordx4 v[46:49], v[224:225], off offset:2048 nt
	global_load_dwordx4 v[50:53], v[224:225], off offset:3072 nt
	v_lshl_add_u64 v[224:225], v[224:225], 0, s[42:43]
	s_mov_b64 exec, s[74:75]
	global_load_dwordx4 v[54:57], v[224:225], off nt
	s_mov_b64 exec, -1
	s_add_i32 s48, s18, 4
	s_mul_i32 s40, s48, 0x3100
	s_mul_hi_u32 s41, s48, 0x3100
	s_add_u32 s40, s16, s40
	s_addc_u32 s41, s17, s41
	v_lshl_add_u64 v[224:225], s[40:41], 0, v[148:149]
	global_load_dwordx4 v[58:61], v[224:225], off nt
	global_load_dwordx4 v[62:65], v[224:225], off offset:1024 nt
	global_load_dwordx4 v[66:69], v[224:225], off offset:2048 nt
	global_load_dwordx4 v[70:73], v[224:225], off offset:3072 nt
	v_lshl_add_u64 v[224:225], v[224:225], 0, s[42:43]
	global_load_dwordx4 v[74:77], v[224:225], off nt
	global_load_dwordx4 v[78:81], v[224:225], off offset:1024 nt
	global_load_dwordx4 v[82:85], v[224:225], off offset:2048 nt
	global_load_dwordx4 v[86:89], v[224:225], off offset:3072 nt
	v_lshl_add_u64 v[224:225], v[224:225], 0, s[42:43]
	global_load_dwordx4 v[90:93], v[224:225], off nt
	global_load_dwordx4 v[94:97], v[224:225], off offset:1024 nt
	global_load_dwordx4 v[98:101], v[224:225], off offset:2048 nt
	global_load_dwordx4 v[102:105], v[224:225], off offset:3072 nt
	v_lshl_add_u64 v[224:225], v[224:225], 0, s[42:43]
	s_mov_b64 exec, s[74:75]
	global_load_dwordx4 v[106:109], v[224:225], off nt
	s_mov_b64 exec, -1
	s_add_i32 s48, s18, 8
	s_mul_i32 s40, s48, 0x3100
	s_mul_hi_u32 s41, s48, 0x3100
	s_add_u32 s40, s16, s40
	s_addc_u32 s41, s17, s41
	v_lshl_add_u64 v[224:225], s[40:41], 0, v[148:149]
	global_load_dwordx4 v[172:175], v[224:225], off nt
	global_load_dwordx4 v[176:179], v[224:225], off offset:1024 nt
	global_load_dwordx4 v[180:183], v[224:225], off offset:2048 nt
	global_load_dwordx4 v[184:187], v[224:225], off offset:3072 nt
	v_lshl_add_u64 v[224:225], v[224:225], 0, s[42:43]
	global_load_dwordx4 v[188:191], v[224:225], off nt
	global_load_dwordx4 v[192:195], v[224:225], off offset:1024 nt
	global_load_dwordx4 v[196:199], v[224:225], off offset:2048 nt
	global_load_dwordx4 v[200:203], v[224:225], off offset:3072 nt
	v_lshl_add_u64 v[224:225], v[224:225], 0, s[42:43]
	global_load_dwordx4 v[204:207], v[224:225], off nt
	global_load_dwordx4 v[208:211], v[224:225], off offset:1024 nt
	global_load_dwordx4 v[212:215], v[224:225], off offset:2048 nt
	global_load_dwordx4 v[216:219], v[224:225], off offset:3072 nt
	v_lshl_add_u64 v[224:225], v[224:225], 0, s[42:43]
	s_mov_b64 exec, s[74:75]
	global_load_dwordx4 v[220:223], v[224:225], off nt
	s_mov_b64 exec, -1
	s_mov_b32 s39, 9
.Lr2l0_loop:
	s_cmp_lt_i32 s18, 8
	s_cbranch_scc1 .Lr2l0_free0
	s_add_i32 s44, s18, -7
	s_mov_b32 s45, 0
	v_mov_b32_e32 v226, 0x18820
.Lr2l0_spin0:
	ds_read_b128 v[228:231], v226
	s_waitcnt lgkmcnt(0)
	v_min3_u32 v227, v228, v229, v230
	v_min_u32_e32 v227, v227, v231
	v_cmp_le_u32_e32 vcc, s44, v227
	s_cbranch_vccnz .Lr2l0_free0
	s_add_i32 s45, s45, 1
	s_cmp_gt_u32 s45, 0x400000
	s_cbranch_scc1 .Lr2l0_free0
	s_sleep 1
	s_branch .Lr2l0_spin0
.Lr2l0_free0:
	s_and_b32 s46, s18, 7
	s_mul_i32 s47, s46, 0x3100
	v_add_u32_e32 v226, s47, v160
	s_waitcnt vmcnt(26)
	ds_write_b128 v226, v[6:9]
	ds_write_b128 v226, v[10:13] offset:1024
	ds_write_b128 v226, v[14:17] offset:2048
	ds_write_b128 v226, v[18:21] offset:3072
	ds_write_b128 v226, v[22:25] offset:4096
	ds_write_b128 v226, v[26:29] offset:5120
	ds_write_b128 v226, v[30:33] offset:6144
	ds_write_b128 v226, v[34:37] offset:7168
	ds_write_b128 v226, v[38:41] offset:8192
	ds_write_b128 v226, v[42:45] offset:9216
	ds_write_b128 v226, v[46:49] offset:10240
	ds_write_b128 v226, v[50:53] offset:11264
	s_mov_b64 exec, s[74:75]
	ds_write_b128 v226, v[54:57] offset:12288
	s_mov_b64 exec, -1
	s_lshl_b32 s46, s46, 2
	s_add_i32 s46, s46, 0x18800
	s_add_i32 s47, s18, 1
	v_mov_b32_e32 v227, s46
	v_mov_b32_e32 v228, s47
	s_waitcnt lgkmcnt(0)
	s_mov_b64 exec, s[72:73]
	ds_write_b32 v227, v228
	s_mov_b64 exec, -1
	s_add_i32 s48, s18, 12
	s_mul_i32 s40, s48, 0x3100
	s_mul_hi_u32 s41, s48, 0x3100
	s_add_u32 s40, s16, s40
	s_addc_u32 s41, s17, s41
	v_lshl_add_u64 v[224:225], s[40:41], 0, v[148:149]
	global_load_dwordx4 v[6:9], v[224:225], off nt
	global_load_dwordx4 v[10:13], v[224:225], off offset:1024 nt
	global_load_dwordx4 v[14:17], v[224:225], off offset:2048 nt
	global_load_dwordx4 v[18:21], v[224:225], off offset:3072 nt
	v_lshl_add_u64 v[224:225], v[224:225], 0, s[42:43]
	global_load_dwordx4 v[22:25], v[224:225], off nt
	global_load_dwordx4 v[26:29], v[224:225], off offset:1024 nt
	global_load_dwordx4 v[30:33], v[224:225], off offset:2048 nt
	global_load_dwordx4 v[34:37], v[224:225], off offset:3072 nt
	v_lshl_add_u64 v[224:225], v[224:225], 0, s[42:43]
	global_load_dwordx4 v[38:41], v[224:225], off nt
	global_load_dwordx4 v[42:45], v[224:225], off offset:1024 nt
	global_load_dwordx4 v[46:49], v[224:225], off offset:2048 nt
	global_load_dwordx4 v[50:53], v[224:225], off offset:3072 nt
	v_lshl_add_u64 v[224:225], v[224:225], 0, s[42:43]
	s_mov_b64 exec, s[74:75]
	global_load_dwordx4 v[54:57], v[224:225], off nt
	s_mov_b64 exec, -1
	s_add_i32 s18, s18, 4
	s_cmp_lt_i32 s18, 8
	s_cbranch_scc1 .Lr2l0_free1
	s_add_i32 s44, s18, -7
	s_mov_b32 s45, 0
	v_mov_b32_e32 v226, 0x18820

; #define LAS __attribute__((address_space(3)))
; DI void rwkv_r2_unit(const Args& A, LAS unsigned char* lds, int u, int tid, int wave, int lane) {
;     ...
;     if (wave >= 4) {
;         const int j = wave - 4; u32x4_t cur[13], nxt[13];
;         rk_pkg_fetch(cur, pkg0 + (size_t)j * PKG_BYTES, lane);
;         for (int cc = j; cc < 128; cc += 4) {
;             if (cc + 4 < 128) rk_pkg_fetch(nxt, pkg0 + (size_t)(cc + 4) * PKG_BYTES, lane);
;             if (cc >= R2_SLOTS) { const unsigned need = (unsigned)(cc - R2_SLOTS + 1); unsigned spins = 0;
;                 for (;;) { const unsigned c0 = consumed[0], c1 = consumed[1], c2 = consumed[2], c3 = consumed[3];
;                     if (c0 >= need && c1 >= need && c2 >= need && c3 >= need) break; if (++spins > (1u << 22)) break; __builtin_amdgcn_s_sleep(1); } }
;             LAS unsigned char* slot = lds + (cc & (R2_SLOTS - 1)) * PKG_BYTES;
; #pragma unroll
;             for (int i = 0; i < 12; ++i) *(LAS u32x4_t*)(slot + i * 1024 + lane * 16) = cur[i];
;             if (lane < 16) *(LAS u32x4_t*)(slot + 12288 + lane * 16) = cur[12];
;             asm volatile("s_waitcnt lgkmcnt(0)" ::: "memory");
;             if (lane == 0) ready[cc & (R2_SLOTS - 1)] = (unsigned)(cc + 1);
;             asm volatile("" ::: "memory");
; #pragma unroll
;             for (int i = 0; i < 13; ++i) cur[i] = nxt[i];
;         }
.Lr2l0_free1:
	s_and_b32 s46, s18, 7
	s_mul_i32 s47, s46, 0x3100
	v_add_u32_e32 v226, s47, v160
	s_waitcnt vmcnt(26)
	ds_write_b128 v226, v[58:61]
	ds_write_b128 v226, v[62:65] offset:1024
	ds_write_b128 v226, v[66:69] offset:2048
	ds_write_b128 v226, v[70:73] offset:3072
	ds_write_b128 v226, v[74:77] offset:4096
	ds_write_b128 v226, v[78:81] offset:5120
	ds_write_b128 v226, v[82:85] offset:6144
	ds_write_b128 v226, v[86:89] offset:7168
	ds_write_b128 v226, v[90:93] offset:8192
	ds_write_b128 v226, v[94:97] offset:9216
	ds_write_b128 v226, v[98:101] offset:10240
	ds_write_b128 v226, v[102:105] offset:11264
	s_mov_b64 exec, s[74:75]
	ds_write_b128 v226, v[106:109] offset:12288
	s_mov_b64 exec, -1
	s_lshl_b32 s46, s46, 2
	s_add_i32 s46, s46, 0x18800
	s_add_i32 s47, s18, 1
	v_mov_b32_e32 v227, s46
	v_mov_b32_e32 v228, s47
	s_waitcnt lgkmcnt(0)
	s_mov_b64 exec, s[72:73]
	ds_write_b32 v227, v228
	s_mov_b64 exec, -1
	s_add_i32 s48, s18, 12
	s_mul_i32 s40, s48, 0x3100
	s_mul_hi_u32 s41, s48, 0x3100
	s_add_u32 s40, s16, s40
	s_addc_u32 s41, s17, s41
	v_lshl_add_u64 v[224:225], s[40:41], 0, v[148:149]
	global_load_dwordx4 v[58:61], v[224:225], off nt
	global_load_dwordx4 v[62:65], v[224:225], off offset:1024 nt
	global_load_dwordx4 v[66:69], v[224:225], off offset:2048 nt
	global_load_dwordx4 v[70:73], v[224:225], off offset:3072 nt
	v_lshl_add_u64 v[224:225], v[224:225], 0, s[42:43]
	global_load_dwordx4 v[74:77], v[224:225], off nt
	global_load_dwordx4 v[78:81], v[224:225], off offset:1024 nt
	global_load_dwordx4 v[82:85], v[224:225], off offset:2048 nt
	global_load_dwordx4 v[86:89], v[224:225], off offset:3072 nt
	v_lshl_add_u64 v[224:225], v[224:225], 0, s[42:43]
	global_load_dwordx4 v[90:93], v[224:225], off nt
	global_load_dwordx4 v[94:97], v[224:225], off offset:1024 nt
	global_load_dwordx4 v[98:101], v[224:225], off offset:2048 nt
	global_load_dwordx4 v[102:105], v[224:225], off offset:3072 nt
	v_lshl_add_u64 v[224:225], v[224:225], 0, s[42:43]
	s_mov_b64 exec, s[74:75]
	global_load_dwordx4 v[106:109], v[224:225], off nt
	s_mov_b64 exec, -1
	s_add_i32 s18, s18, 4
	s_cmp_lt_i32 s18, 8
	s_cbranch_scc1 .Lr2l0_free2
	s_add_i32 s44, s18, -7
	s_mov_b32 s45, 0
	v_mov_b32_e32 v226, 0x18820

; #define LAS __attribute__((address_space(3)))
; DI void rwkv_r2_unit(const Args& A, LAS unsigned char* lds, int u, int tid, int wave, int lane) {
;     ...
;     if (wave >= 4) {
;         const int j = wave - 4; u32x4_t cur[13], nxt[13];
;         rk_pkg_fetch(cur, pkg0 + (size_t)j * PKG_BYTES, lane);
;         for (int cc = j; cc < 128; cc += 4) {
;             if (cc + 4 < 128) rk_pkg_fetch(nxt, pkg0 + (size_t)(cc + 4) * PKG_BYTES, lane);
;             if (cc >= R2_SLOTS) { const unsigned need = (unsigned)(cc - R2_SLOTS + 1); unsigned spins = 0;
;                 for (;;) { const unsigned c0 = consumed[0], c1 = consumed[1], c2 = consumed[2], c3 = consumed[3];
;                     if (c0 >= need && c1 >= need && c2 >= need && c3 >= need) break; if (++spins > (1u << 22)) break; __builtin_amdgcn_s_sleep(1); } }
;             LAS unsigned char* slot = lds + (cc & (R2_SLOTS - 1)) * PKG_BYTES;
; #pragma unroll
;             for (int i = 0; i < 12; ++i) *(LAS u32x4_t*)(slot + i * 1024 + lane * 16) = cur[i];
;             if (lane < 16) *(LAS u32x4_t*)(slot + 12288 + lane * 16) = cur[12];
;             asm volatile("s_waitcnt lgkmcnt(0)" ::: "memory");
;             if (lane == 0) ready[cc & (R2_SLOTS - 1)] = (unsigned)(cc + 1);
;             asm volatile("" ::: "memory");
; #pragma unroll
;             for (int i = 0; i < 13; ++i) cur[i] = nxt[i];
;         }
.Lr2l0_free2:
	s_and_b32 s46, s18, 7
	s_mul_i32 s47, s46, 0x3100
	v_add_u32_e32 v226, s47, v160
	s_waitcnt vmcnt(26)
	ds_write_b128 v226, v[172:175]
	ds_write_b128 v226, v[176:179] offset:1024
	ds_write_b128 v226, v[180:183] offset:2048
	ds_write_b128 v226, v[184:187] offset:3072
	ds_write_b128 v226, v[188:191] offset:4096
	ds_write_b128 v226, v[192:195] offset:5120
	ds_write_b128 v226, v[196:199] offset:6144
	ds_write_b128 v226, v[200:203] offset:7168
	ds_write_b128 v226, v[204:207] offset:8192
	ds_write_b128 v226, v[208:211] offset:9216
	ds_write_b128 v226, v[212:215] offset:10240
	ds_write_b128 v226, v[216:219] offset:11264
	s_mov_b64 exec, s[74:75]
	ds_write_b128 v226, v[220:223] offset:12288
	s_mov_b64 exec, -1
	s_lshl_b32 s46, s46, 2
	s_add_i32 s46, s46, 0x18800
	s_add_i32 s47, s18, 1
	v_mov_b32_e32 v227, s46
	v_mov_b32_e32 v228, s47
	s_waitcnt lgkmcnt(0)
	s_mov_b64 exec, s[72:73]
	ds_write_b32 v227, v228
	s_mov_b64 exec, -1
	s_add_i32 s48, s18, 12
	s_mul_i32 s40, s48, 0x3100
	s_mul_hi_u32 s41, s48, 0x3100
	s_add_u32 s40, s16, s40
	s_addc_u32 s41, s17, s41
	v_lshl_add_u64 v[224:225], s[40:41], 0, v[148:149]
	global_load_dwordx4 v[172:175], v[224:225], off nt
	global_load_dwordx4 v[176:179], v[224:225], off offset:1024 nt
	global_load_dwordx4 v[180:183], v[224:225], off offset:2048 nt
	global_load_dwordx4 v[184:187], v[224:225], off offset:3072 nt
	v_lshl_add_u64 v[224:225], v[224:225], 0, s[42:43]
	global_load_dwordx4 v[188:191], v[224:225], off nt
	global_load_dwordx4 v[192:195], v[224:225], off offset:1024 nt
	global_load_dwordx4 v[196:199], v[224:225], off offset:2048 nt
	global_load_dwordx4 v[200:203], v[224:225], off offset:3072 nt
	v_lshl_add_u64 v[224:225], v[224:225], 0, s[42:43]
	global_load_dwordx4 v[204:207], v[224:225], off nt
	global_load_dwordx4 v[208:211], v[224:225], off offset:1024 nt
	global_load_dwordx4 v[212:215], v[224:225], off offset:2048 nt
	global_load_dwordx4 v[216:219], v[224:225], off offset:3072 nt
	v_lshl_add_u64 v[224:225], v[224:225], 0, s[42:43]
	s_mov_b64 exec, s[74:75]
	global_load_dwordx4 v[220:223], v[224:225], off nt
	s_mov_b64 exec, -1
	s_add_i32 s18, s18, 4
	s_add_i32 s39, s39, -1
	s_cmp_lg_u32 s39, 0
	s_cbranch_scc1 .Lr2l0_loop
	s_cmp_lt_i32 s18, 8
	s_cbranch_scc1 .Lr2l0_free3
	s_add_i32 s44, s18, -7
	s_mov_b32 s45, 0
	v_mov_b32_e32 v226, 0x18820

; #define LAS __attribute__((address_space(3)))
; DI void rwkv_r2_unit(const Args& A, LAS unsigned char* lds, int u, int tid, int wave, int lane) {
;     ...
;             if (cc >= R2_SLOTS) { const unsigned need = (unsigned)(cc - R2_SLOTS + 1); unsigned spins = 0;
;                 for (;;) { const unsigned c0 = consumed[0], c1 = consumed[1], c2 = consumed[2], c3 = consumed[3];
;                     if (c0 >= need && c1 >= need && c2 >= need && c3 >= need) break; if (++spins > (1u << 22)) break; __builtin_amdgcn_s_sleep(1); } }
;             LAS unsigned char* slot = lds + (cc & (R2_SLOTS - 1)) * PKG_BYTES;
; #pragma unroll
;             for (int i = 0; i < 12; ++i) *(LAS u32x4_t*)(slot + i * 1024 + lane * 16) = cur[i];
;             if (lane < 16) *(LAS u32x4_t*)(slot + 12288 + lane * 16) = cur[12];
;             asm volatile("s_waitcnt lgkmcnt(0)" ::: "memory");
;             if (lane == 0) ready[cc & (R2_SLOTS - 1)] = (unsigned)(cc + 1);
;             asm volatile("" ::: "memory");
.Lr2l0_free5:
	s_and_b32 s46, s18, 7
	s_mul_i32 s47, s46, 0x3100
	v_add_u32_e32 v226, s47, v160
	s_waitcnt vmcnt(26)
	ds_write_b128 v226, v[172:175]
	ds_write_b128 v226, v[176:179] offset:1024
	ds_write_b128 v226, v[180:183] offset:2048
	ds_write_b128 v226, v[184:187] offset:3072
	ds_write_b128 v226, v[188:191] offset:4096
	ds_write_b128 v226, v[192:195] offset:5120
	ds_write_b128 v226, v[196:199] offset:6144
	ds_write_b128 v226, v[200:203] offset:7168
	ds_write_b128 v226, v[204:207] offset:8192
	ds_write_b128 v226, v[208:211] offset:9216
	ds_write_b128 v226, v[212:215] offset:10240
	ds_write_b128 v226, v[216:219] offset:11264
	s_mov_b64 exec, s[74:75]
	ds_write_b128 v226, v[220:223] offset:12288
	s_mov_b64 exec, -1
	s_lshl_b32 s46, s46, 2
	s_add_i32 s46, s46, 0x18800
	s_add_i32 s47, s18, 1
	v_mov_b32_e32 v227, s46
	v_mov_b32_e32 v228, s47
	s_waitcnt lgkmcnt(0)
	s_mov_b64 exec, s[72:73]
	ds_write_b32 v227, v228
	s_mov_b64 exec, -1
	s_add_i32 s18, s18, 4
	s_cmp_lt_i32 s18, 8
	s_cbranch_scc1 .Lr2l0_free6
	s_add_i32 s44, s18, -7
	s_mov_b32 s45, 0
	v_mov_b32_e32 v226, 0x18820

; #define LAS __attribute__((address_space(3)))
; DI void rwkv_r2_unit(const Args& A, LAS unsigned char* lds, int u, int tid, int wave, int lane) {
;     ...
;             if (cc >= R2_SLOTS) { const unsigned need = (unsigned)(cc - R2_SLOTS + 1); unsigned spins = 0;
;                 for (;;) { const unsigned c0 = consumed[0], c1 = consumed[1], c2 = consumed[2], c3 = consumed[3];
;                     if (c0 >= need && c1 >= need && c2 >= need && c3 >= need) break; if (++spins > (1u << 22)) break; __builtin_amdgcn_s_sleep(1); } }
;             LAS unsigned char* slot = lds + (cc & (R2_SLOTS - 1)) * PKG_BYTES;
; #pragma unroll
;             for (int i = 0; i < 12; ++i) *(LAS u32x4_t*)(slot + i * 1024 + lane * 16) = cur[i];
;             if (lane < 16) *(LAS u32x4_t*)(slot + 12288 + lane * 16) = cur[12];
;             asm volatile("s_waitcnt lgkmcnt(0)" ::: "memory");
;             if (lane == 0) ready[cc & (R2_SLOTS - 1)] = (unsigned)(cc + 1);
;             asm volatile("" ::: "memory");
.Lr2l0_free6:
	s_and_b32 s46, s18, 7
	s_mul_i32 s47, s46, 0x3100
	v_add_u32_e32 v226, s47, v160
	s_waitcnt vmcnt(13)
	ds_write_b128 v226, v[6:9]
	ds_write_b128 v226, v[10:13] offset:1024
	ds_write_b128 v226, v[14:17] offset:2048
	ds_write_b128 v226, v[18:21] offset:3072
	ds_write_b128 v226, v[22:25] offset:4096
	ds_write_b128 v226, v[26:29] offset:5120
	ds_write_b128 v226, v[30:33] offset:6144
	ds_write_b128 v226, v[34:37] offset:7168
	ds_write_b128 v226, v[38:41] offset:8192
	ds_write_b128 v226, v[42:45] offset:9216
	ds_write_b128 v226, v[46:49] offset:10240
	ds_write_b128 v226, v[50:53] offset:11264
	s_mov_b64 exec, s[74:75]
	ds_write_b128 v226, v[54:57] offset:12288
	s_mov_b64 exec, -1
	s_lshl_b32 s46, s46, 2
	s_add_i32 s46, s46, 0x18800
	s_add_i32 s47, s18, 1
	v_mov_b32_e32 v227, s46
	v_mov_b32_e32 v228, s47
	s_waitcnt lgkmcnt(0)
	s_mov_b64 exec, s[72:73]
	ds_write_b32 v227, v228
	s_mov_b64 exec, -1
	s_add_i32 s18, s18, 4
	s_cmp_lt_i32 s18, 8
	s_cbranch_scc1 .Lr2l0_free7
	s_add_i32 s44, s18, -7
	s_mov_b32 s45, 0
	v_mov_b32_e32 v226, 0x18820

; #define LAS __attribute__((address_space(3)))
; DI void rwkv_r2_unit(const Args& A, LAS unsigned char* lds, int u, int tid, int wave, int lane) {
;     ...
;             LAS unsigned char* slot = lds + (cc & (R2_SLOTS - 1)) * PKG_BYTES;
; #pragma unroll
;             for (int i = 0; i < 12; ++i) *(LAS u32x4_t*)(slot + i * 1024 + lane * 16) = cur[i];
;             if (lane < 16) *(LAS u32x4_t*)(slot + 12288 + lane * 16) = cur[12];
;             asm volatile("s_waitcnt lgkmcnt(0)" ::: "memory");
;             if (lane == 0) ready[cc & (R2_SLOTS - 1)] = (unsigned)(cc + 1);
;             asm volatile("" ::: "memory");
.Lr2l0_free7:
	s_and_b32 s46, s18, 7
	s_mul_i32 s47, s46, 0x3100
	v_add_u32_e32 v226, s47, v160
	s_waitcnt vmcnt(0)
	ds_write_b128 v226, v[58:61]
	ds_write_b128 v226, v[62:65] offset:1024
	ds_write_b128 v226, v[66:69] offset:2048
	ds_write_b128 v226, v[70:73] offset:3072
	ds_write_b128 v226, v[74:77] offset:4096
	ds_write_b128 v226, v[78:81] offset:5120
	ds_write_b128 v226, v[82:85] offset:6144
	ds_write_b128 v226, v[86:89] offset:7168
	ds_write_b128 v226, v[90:93] offset:8192
	ds_write_b128 v226, v[94:97] offset:9216
	ds_write_b128 v226, v[98:101] offset:10240
	ds_write_b128 v226, v[102:105] offset:11264
	s_mov_b64 exec, s[74:75]
	ds_write_b128 v226, v[106:109] offset:12288
	s_mov_b64 exec, -1
	s_lshl_b32 s46, s46, 2
	s_add_i32 s46, s46, 0x18800
	s_add_i32 s47, s18, 1
	v_mov_b32_e32 v227, s46
	v_mov_b32_e32 v228, s47
	s_waitcnt lgkmcnt(0)
	s_mov_b64 exec, s[72:73]
	ds_write_b32 v227, v228
	s_mov_b64 exec, -1
	s_add_i32 s18, s18, 4
	s_branch .LBB0_642

; #define LAS __attribute__((address_space(3)))
; DI void rk_pkg_fetch(u32x4_t (&buf)[13], const unsigned char* pkg, int lane) {
; #pragma unroll
;     for (int i = 0; i < 12; ++i) buf[i] = __builtin_nontemporal_load((const u32x4_t*)(pkg + i * 1024 + lane * 16));
;     buf[12] = (lane < 16) ? __builtin_nontemporal_load((const u32x4_t*)(pkg + 12288 + lane * 16)) : (u32x4_t){0u, 0u, 0u, 0u};
; }
; DI void rwkv_r2_unit(const Args& A, LAS unsigned char* lds, int u, int tid, int wave, int lane) {
;     ...
;     const unsigned char* pkg0 = A.ws + WS_PKG + ((size_t)((dir * NB + b) * 6 + hh) * 128) * PKG_BYTES;
;     volatile LAS unsigned* ready = (volatile LAS unsigned*)(lds + R2_CTL); volatile LAS unsigned* consumed = ready + 8;
;     __syncthreads();
;     if (tid < 16) ready[tid] = 0u;
;     __syncthreads();
;     if (wave >= 4) {
;         const int j = wave - 4; u32x4_t cur[13], nxt[13];
;         rk_pkg_fetch(cur, pkg0 + (size_t)j * PKG_BYTES, lane);
;         for (int cc = j; cc < 128; cc += 4) {
;             if (cc + 4 < 128) rk_pkg_fetch(nxt, pkg0 + (size_t)(cc + 4) * PKG_BYTES, lane);
.LBB0_2143:
	s_and_b64 vcc, exec, s[10:11]
	s_cbranch_vccz .LBB0_2104
	s_lshl_b32 s10, s14, 3
	s_add_i32 s10, s10, s36
	s_mul_i32 s10, s10, 6
	s_add_i32 s10, s10, s37
	s_mul_hi_i32 s11, s10, 0x188000
	s_mul_i32 s10, s10, 0x188000
	s_add_u32 s16, s27, s10
	s_addc_u32 s17, s28, s11
	s_add_u32 s10, s16, s26
	s_addc_u32 s11, s17, s23
	v_readlane_b32 s18, v235, 52
	v_cmp_eq_u32_e64 s[72:73], 0, v146
	v_cmp_gt_u32_e64 s[74:75], 16, v146
	s_mov_b64 s[42:43], 0x1000
	s_nop 2
	s_add_i32 s18, s18, -4
	s_waitcnt vmcnt(0)
	s_mul_i32 s40, s18, 0x3100
	s_mul_hi_u32 s41, s18, 0x3100
	s_add_u32 s40, s16, s40
	s_addc_u32 s41, s17, s41
	v_lshl_add_u64 v[224:225], s[40:41], 0, v[148:149]
	global_load_dwordx4 v[6:9], v[224:225], off nt
	global_load_dwordx4 v[10:13], v[224:225], off offset:1024 nt
	global_load_dwordx4 v[14:17], v[224:225], off offset:2048 nt
	global_load_dwordx4 v[18:21], v[224:225], off offset:3072 nt
	v_lshl_add_u64 v[224:225], v[224:225], 0, s[42:43]
	global_load_dwordx4 v[22:25], v[224:225], off nt
	global_load_dwordx4 v[26:29], v[224:225], off offset:1024 nt
	global_load_dwordx4 v[30:33], v[224:225], off offset:2048 nt
	global_load_dwordx4 v[34:37], v[224:225], off offset:3072 nt
	v_lshl_add_u64 v[224:225], v[224:225], 0, s[42:43]
	global_load_dwordx4 v[38:41], v[224:225], off nt
	global_load_dwordx4 v[42:45], v[224:225], off offset:1024 nt
	global_load_dwordx4 v[46:49], v[224:225], off offset:2048 nt
	global_load_dwordx4 v[50:53], v[224:225], off offset:3072 nt
	v_lshl_add_u64 v[224:225], v[224:225], 0, s[42:43]
	s_mov_b64 exec, s[74:75]
	global_load_dwordx4 v[54:57], v[224:225], off nt
	s_mov_b64 exec, -1
	s_add_i32 s48, s18, 4
	s_mul_i32 s40, s48, 0x3100
	s_mul_hi_u32 s41, s48, 0x3100
	s_add_u32 s40, s16, s40
	s_addc_u32 s41, s17, s41
	v_lshl_add_u64 v[224:225], s[40:41], 0, v[148:149]
	global_load_dwordx4 v[58:61], v[224:225], off nt
	global_load_dwordx4 v[62:65], v[224:225], off offset:1024 nt
	global_load_dwordx4 v[66:69], v[224:225], off offset:2048 nt
	global_load_dwordx4 v[70:73], v[224:225], off offset:3072 nt
	v_lshl_add_u64 v[224:225], v[224:225], 0, s[42:43]
	global_load_dwordx4 v[74:77], v[224:225], off nt
	global_load_dwordx4 v[78:81], v[224:225], off offset:1024 nt
	global_load_dwordx4 v[82:85], v[224:225], off offset:2048 nt
	global_load_dwordx4 v[86:89], v[224:225], off offset:3072 nt
	v_lshl_add_u64 v[224:225], v[224:225], 0, s[42:43]
	global_load_dwordx4 v[90:93], v[224:225], off nt
	global_load_dwordx4 v[94:97], v[224:225], off offset:1024 nt
	global_load_dwordx4 v[98:101], v[224:225], off offset:2048 nt
	global_load_dwordx4 v[102:105], v[224:225], off offset:3072 nt
	v_lshl_add_u64 v[224:225], v[224:225], 0, s[42:43]
	s_mov_b64 exec, s[74:75]
	global_load_dwordx4 v[106:109], v[224:225], off nt
	s_mov_b64 exec, -1
	s_add_i32 s48, s18, 8
	s_mul_i32 s40, s48, 0x3100
	s_mul_hi_u32 s41, s48, 0x3100
	s_add_u32 s40, s16, s40
	s_addc_u32 s41, s17, s41
	v_lshl_add_u64 v[224:225], s[40:41], 0, v[148:149]
	global_load_dwordx4 v[172:175], v[224:225], off nt
	global_load_dwordx4 v[176:179], v[224:225], off offset:1024 nt
	global_load_dwordx4 v[180:183], v[224:225], off offset:2048 nt
	global_load_dwordx4 v[184:187], v[224:225], off offset:3072 nt
	v_lshl_add_u64 v[224:225], v[224:225], 0, s[42:43]
	global_load_dwordx4 v[188:191], v[224:225], off nt
	global_load_dwordx4 v[192:195], v[224:225], off offset:1024 nt
	global_load_dwordx4 v[196:199], v[224:225], off offset:2048 nt
	global_load_dwordx4 v[200:203], v[224:225], off offset:3072 nt
	v_lshl_add_u64 v[224:225], v[224:225], 0, s[42:43]
	global_load_dwordx4 v[204:207], v[224:225], off nt
	global_load_dwordx4 v[208:211], v[224:225], off offset:1024 nt
	global_load_dwordx4 v[212:215], v[224:225], off offset:2048 nt
	global_load_dwordx4 v[216:219], v[224:225], off offset:3072 nt
	v_lshl_add_u64 v[224:225], v[224:225], 0, s[42:43]
	s_mov_b64 exec, s[74:75]
	global_load_dwordx4 v[220:223], v[224:225], off nt
	s_mov_b64 exec, -1
	s_mov_b32 s39, 9
